# cb1b_early_V_reads_before_rescale_test
# baseline (speedup 1.0000x reference)
; __device__ __forceinline__ void qkt64c(f32x16& p0, f32x16& p1, const char* Ks, const bf16x8* qr, const f32x16& cinit, int r32, int hi) {
; #pragma unroll
;     for (int d0 = 0; d0 < 4; ++d0) { const int cb = (d0 * 16 + hi * 8) * 2;
;         const bf16x8 b0 = *reinterpret_cast<const bf16x8*>(Ks + kswz<64>(r32, cb));
;         const bf16x8 b1 = *reinterpret_cast<const bf16x8*>(Ks + kswz<64>(32 + r32, cb));
;         if (d0 == 0) { p0 = __builtin_amdgcn_mfma_f32_32x32x16_bf16(b0, qr[0], cinit, 0, 0, 0); p1 = __builtin_amdgcn_mfma_f32_32x32x16_bf16(b1, qr[0], cinit, 0, 0, 0); }
;         else { p0 = __builtin_amdgcn_mfma_f32_32x32x16_bf16(b0, qr[d0], p0, 0, 0, 0); p1 = __builtin_amdgcn_mfma_f32_32x32x16_bf16(b1, qr[d0], p1, 0, 0, 0); } }
; }
.LBB0_823:
	s_lshl_b32 s2, s42, 13
	s_add_i32 s2, s2, 0
	v_add_u32_e32 v128, s2, v223
	ds_read_b128 v[144:147], v128 offset:49152
	v_add_u32_e32 v129, s2, v226
	ds_read_b128 v[148:151], v129 offset:49152
	v_add_u32_e32 v130, s2, v228
	ds_read_b128 v[152:155], v130 offset:49152
	v_add_u32_e32 v131, s2, v229
	ds_read_b128 v[156:159], v131 offset:49152
	ds_read_b128 v[232:235], v128 offset:53248
	ds_read_b128 v[236:239], v129 offset:53248
	ds_read_b128 v[240:243], v130 offset:53248
	ds_read_b128 v[244:247], v131 offset:53248
	v_lshl_add_u64 v[202:203], v[200:201], 0, s[64:65]
	s_mov_b32 s2, 0x8a40000
	v_add_co_u32_e32 v64, vcc, s2, v202
	s_mov_b32 s2, 0x8a50000
	s_nop 0
	v_addc_co_u32_e32 v65, vcc, 0, v203, vcc
	v_add_co_u32_e32 v66, vcc, s2, v202
	v_lshl_add_u64 v[204:205], v[198:199], 0, s[64:65]
	s_nop 0
	v_addc_co_u32_e32 v67, vcc, 0, v203, vcc
	s_mov_b32 s2, 0x6a40000
	global_load_dwordx4 v[178:181], v[64:65], off
	global_load_dwordx4 v[182:185], v[66:67], off
	v_add_co_u32_e32 v64, vcc, s2, v204
	s_nop 1
	v_addc_co_u32_e32 v65, vcc, 0, v205, vcc
	global_load_dwordx4 v[186:189], v[64:65], off
	v_exp_f32_e32 v190, v120
	v_exp_f32_e32 v191, v121
	v_add_f32_e32 v120, v96, v97
	v_add_f32_e32 v121, v98, v99
	s_waitcnt lgkmcnt(7)
	v_mfma_f32_32x32x16_bf16 v[128:143], v[144:147], v[162:165], v[80:95]
	v_exp_f32_e32 v192, v122
	v_add_f32_e32 v120, v120, v121
	v_add_f32_e32 v121, v100, v101
	v_add_f32_e32 v122, v102, v103
	v_exp_f32_e32 v193, v123
	s_waitcnt lgkmcnt(6)
	v_mfma_f32_32x32x16_bf16 v[128:143], v[148:151], v[166:169], v[128:143]
	v_add_f32_e32 v121, v121, v122
	v_add_f32_e32 v122, v104, v105
	v_add_f32_e32 v123, v106, v107
	v_add_f32_e32 v122, v122, v123
	v_add_f32_e32 v123, v108, v109
	s_waitcnt lgkmcnt(5)
	v_mfma_f32_32x32x16_bf16 v[128:143], v[152:155], v[170:173], v[128:143]
	v_add_f32_e32 v208, v110, v111
	v_add_f32_e32 v123, v123, v208
	v_add_f32_e32 v208, v112, v113
	v_add_f32_e32 v209, v114, v115
	v_add_f32_e32 v208, v208, v209
	s_waitcnt lgkmcnt(4)
	v_mfma_f32_32x32x16_bf16 v[128:143], v[156:159], v[174:177], v[128:143]
	v_exp_f32_e32 v124, v124
	v_exp_f32_e32 v125, v125
	s_waitcnt lgkmcnt(3)
	v_mfma_f32_32x32x16_bf16 v[144:159], v[232:235], v[162:165], v[80:95]
	v_lshl_add_u32 v234, s12, 14, v217
	ds_read_b64_tr_b16 v[64:65], v234 offset:0
	ds_read_b64_tr_b16 v[66:67], v234 offset:0x800
	ds_read_b64_tr_b16 v[68:69], v234 offset:0x1000
	ds_read_b64_tr_b16 v[70:71], v234 offset:0x1800
	ds_read_b64_tr_b16 v[72:73], v234 offset:0x2000
	ds_read_b64_tr_b16 v[74:75], v234 offset:0x2800
	ds_read_b64_tr_b16 v[76:77], v234 offset:0x3000
	ds_read_b64_tr_b16 v[78:79], v234 offset:0x3800
	v_exp_f32_e32 v126, v126
	v_exp_f32_e32 v127, v127
	v_add_f32_e32 v120, v208, v120
	v_add_f32_e32 v208, v116, v117
	v_add_f32_e32 v209, v118, v119
	v_add_f32_e32 v208, v208, v209
	v_add_f32_e32 v121, v208, v121
	s_waitcnt lgkmcnt(10)
	v_mfma_f32_32x32x16_bf16 v[144:159], v[236:239], v[166:169], v[144:159]
	v_add_f32_e32 v208, v190, v191
	v_add_f32_e32 v209, v192, v193
	v_add_f32_e32 v208, v208, v209
	v_add_f32_e32 v122, v122, v208
	v_add_f32_e32 v208, v124, v125
	v_add_f32_e32 v209, v126, v127
	v_add_f32_e32 v208, v208, v209
	s_waitcnt lgkmcnt(9)
	v_mfma_f32_32x32x16_bf16 v[144:159], v[240:243], v[170:173], v[144:159]
	v_add_f32_e32 v123, v123, v208
	v_add_f32_e32 v120, v120, v121
	v_add_f32_e32 v121, v122, v123
	v_add_f32_e32 v231, v120, v121
	v_mov_b32_e32 v232, v231
	v_cvt_pk_bf16_f32 v96, v96, v97
	v_cvt_pk_bf16_f32 v97, v98, v99
	s_waitcnt lgkmcnt(8)
	v_mfma_f32_32x32x16_bf16 v[144:159], v[244:247], v[174:177], v[144:159]
	v_cvt_pk_bf16_f32 v98, v100, v101
	v_cvt_pk_bf16_f32 v99, v102, v103
	v_cvt_pk_bf16_f32 v120, v104, v105
	v_cvt_pk_bf16_f32 v121, v106, v107
	v_cvt_pk_bf16_f32 v122, v108, v109
	v_cvt_pk_bf16_f32 v123, v110, v111
	v_permlane32_swap_b32_e32 v96, v98
	v_permlane32_swap_b32_e32 v97, v99
	v_cvt_pk_bf16_f32 v104, v112, v113
	v_cvt_pk_bf16_f32 v105, v114, v115
	v_cvt_pk_bf16_f32 v106, v116, v117
	v_cvt_pk_bf16_f32 v107, v118, v119
	s_waitcnt lgkmcnt(0)
	v_mfma_f32_32x32x16_bf16 v[0:15], v[96:99], v[64:67], v[0:15]
	v_permlane32_swap_b32_e32 v120, v122
	v_permlane32_swap_b32_e32 v121, v123
	v_cvt_pk_bf16_f32 v100, v190, v191
	v_cvt_pk_bf16_f32 v101, v192, v193
	v_cvt_pk_bf16_f32 v102, v124, v125
	v_cvt_pk_bf16_f32 v103, v126, v127
	v_mfma_f32_32x32x16_bf16 v[0:15], v[120:123], v[68:71], v[0:15]
	v_permlane32_swap_b32_e32 v104, v106
	v_permlane32_swap_b32_e32 v105, v107
	ds_read_b64_tr_b16 v[236:237], v234 offset:0x200
	ds_read_b64_tr_b16 v[238:239], v234 offset:0xa00
	ds_read_b64_tr_b16 v[240:241], v234 offset:0x1200
	ds_read_b64_tr_b16 v[242:243], v234 offset:0x1a00
	ds_read_b64_tr_b16 v[244:245], v234 offset:0x2200
	ds_read_b64_tr_b16 v[246:247], v234 offset:0x2a00
	ds_read_b64_tr_b16 v[190:191], v234 offset:0x3200
	ds_read_b64_tr_b16 v[192:193], v234 offset:0x3a00
	v_mfma_f32_32x32x16_bf16 v[0:15], v[104:107], v[72:75], v[0:15]
	v_permlane32_swap_b32_e32 v100, v102
	v_permlane32_swap_b32_e32 v101, v103
	v_permlane32_swap_b32_e32 v231, v232
	v_max_f32_e32 v108, v128, v129
	v_max3_f32 v109, v130, v131, v145
	v_max3_f32 v108, v108, v144, v146
	v_max3_f32 v108, v108, v147, v132
	v_max3_f32 v109, v109, v134, v135
	v_mfma_f32_32x32x16_bf16 v[0:15], v[100:103], v[76:79], v[0:15]
	v_max3_f32 v208, v108, v133, v148
	v_max3_f32 v209, v109, v150, v151
	ds_read_b64_tr_b16 v[124:125], v234 offset:0x400
	ds_read_b64_tr_b16 v[126:127], v234 offset:0xc00
	ds_read_b64_tr_b16 v[116:117], v234 offset:0x1400
	ds_read_b64_tr_b16 v[118:119], v234 offset:0x1c00
	ds_read_b64_tr_b16 v[112:113], v234 offset:0x2400
	ds_read_b64_tr_b16 v[114:115], v234 offset:0x2c00
	ds_read_b64_tr_b16 v[108:109], v234 offset:0x3400
	ds_read_b64_tr_b16 v[110:111], v234 offset:0x3c00
	s_waitcnt lgkmcnt(8)
	v_mfma_f32_32x32x16_bf16 v[48:63], v[96:99], v[236:239], v[48:63]
	v_max3_f32 v208, v208, v149, v136
	v_max3_f32 v209, v209, v138, v139
	v_max3_f32 v208, v208, v137, v152
	v_max3_f32 v209, v209, v154, v155
	v_max3_f32 v208, v208, v153, v140
	v_max3_f32 v209, v209, v142, v143
	v_max3_f32 v208, v208, v141, v156
	v_mfma_f32_32x32x16_bf16 v[48:63], v[120:123], v[240:243], v[48:63]
	v_max3_f32 v209, v209, v158, v159
	v_max3_f32 v208, v208, v157, v209
	v_mov_b32_e32 v209, v208
	s_nop 1
	v_permlane32_swap_b32_e32 v208, v209
	v_mfma_f32_32x32x16_bf16 v[48:63], v[104:107], v[244:247], v[48:63]
	v_max_f32_e32 v233, v208, v209
	v_mfma_f32_32x32x16_bf16 v[48:63], v[100:103], v[190:193], v[48:63]
	ds_read_b64_tr_b16 v[190:191], v234 offset:0x600
	ds_read_b64_tr_b16 v[192:193], v234 offset:0xe00
	ds_read_b64_tr_b16 v[236:237], v234 offset:0x1600
	ds_read_b64_tr_b16 v[238:239], v234 offset:0x1e00
	ds_read_b64_tr_b16 v[240:241], v234 offset:0x2600
	ds_read_b64_tr_b16 v[242:243], v234 offset:0x2e00
	ds_read_b64_tr_b16 v[244:245], v234 offset:0x3600
	ds_read_b64_tr_b16 v[246:247], v234 offset:0x3e00
	s_mov_b32 s2, 0x4138aa3b
	v_cmp_ge_f32_e32 vcc, s2, v233
	s_cmp_eq_u64 vcc, exec
	s_cbranch_scc0 .LBB0_836
	v_mov_b32_e32 v233, 1.0

; __device__ __forceinline__ void qkt64c(f32x16& p0, f32x16& p1, const char* Ks, const bf16x8* qr, const f32x16& cinit, int r32, int hi) {
; #pragma unroll
;     for (int d0 = 0; d0 < 4; ++d0) { const int cb = (d0 * 16 + hi * 8) * 2;
;         const bf16x8 b0 = *reinterpret_cast<const bf16x8*>(Ks + kswz<64>(r32, cb));
;         const bf16x8 b1 = *reinterpret_cast<const bf16x8*>(Ks + kswz<64>(32 + r32, cb));
;         if (d0 == 0) { p0 = __builtin_amdgcn_mfma_f32_32x32x16_bf16(b0, qr[0], cinit, 0, 0, 0); p1 = __builtin_amdgcn_mfma_f32_32x32x16_bf16(b1, qr[0], cinit, 0, 0, 0); }
;         else { p0 = __builtin_amdgcn_mfma_f32_32x32x16_bf16(b0, qr[d0], p0, 0, 0, 0); p1 = __builtin_amdgcn_mfma_f32_32x32x16_bf16(b1, qr[d0], p1, 0, 0, 0); } }
; }
.LBB0_846:
	s_lshl_b32 s2, s30, 13
	s_add_i32 s2, s2, 0
	v_add_u32_e32 v128, s2, v227
	ds_read_b128 v[144:147], v128 offset:49152
	v_add_u32_e32 v129, s2, v231
	ds_read_b128 v[148:151], v129 offset:49152
	v_add_u32_e32 v130, s2, v232
	ds_read_b128 v[152:155], v130 offset:49152
	v_add_u32_e32 v131, s2, v233
	ds_read_b128 v[156:159], v131 offset:49152
	ds_read_b128 v[190:193], v128 offset:53248
	ds_read_b128 v[236:239], v129 offset:53248
	ds_read_b128 v[240:243], v130 offset:53248
	ds_read_b128 v[244:247], v131 offset:53248
	v_lshl_add_u64 v[202:203], v[200:201], 0, s[64:65]
	s_mov_b32 s2, 0x8a40000
	v_add_co_u32_e32 v64, vcc, s2, v202
	s_mov_b32 s2, 0x8a50000
	s_nop 0
	v_addc_co_u32_e32 v65, vcc, 0, v203, vcc
	v_add_co_u32_e32 v66, vcc, s2, v202
	v_lshl_add_u64 v[204:205], v[198:199], 0, s[64:65]
	s_nop 0
	v_addc_co_u32_e32 v67, vcc, 0, v203, vcc
	s_mov_b32 s2, 0x6a40000
	global_load_dwordx4 v[178:181], v[64:65], off
	global_load_dwordx4 v[182:185], v[66:67], off
	v_add_co_u32_e32 v64, vcc, s2, v204
	s_nop 1
	v_addc_co_u32_e32 v65, vcc, 0, v205, vcc
	global_load_dwordx4 v[186:189], v[64:65], off offset:128
	v_exp_f32_e32 v208, v120
	v_exp_f32_e32 v209, v121
	v_add_f32_e32 v120, v96, v97
	v_add_f32_e32 v121, v98, v99
	s_waitcnt lgkmcnt(7)
	v_mfma_f32_32x32x16_bf16 v[128:143], v[144:147], v[162:165], v[80:95]
	v_exp_f32_e32 v210, v122
	v_add_f32_e32 v120, v120, v121
	v_add_f32_e32 v121, v100, v101
	v_add_f32_e32 v122, v102, v103
	v_exp_f32_e32 v211, v123
	s_waitcnt lgkmcnt(6)
	v_mfma_f32_32x32x16_bf16 v[128:143], v[148:151], v[166:169], v[128:143]
	v_add_f32_e32 v121, v121, v122
	v_add_f32_e32 v122, v104, v105
	v_add_f32_e32 v123, v106, v107
	v_add_f32_e32 v122, v122, v123
	v_add_f32_e32 v123, v108, v109
	s_waitcnt lgkmcnt(5)
	v_mfma_f32_32x32x16_bf16 v[128:143], v[152:155], v[170:173], v[128:143]
	v_exp_f32_e32 v124, v124
	v_exp_f32_e32 v125, v125
	v_exp_f32_e32 v126, v126
	v_exp_f32_e32 v127, v127
	v_cvt_pk_bf16_f32 v96, v96, v97
	s_waitcnt lgkmcnt(4)
	v_mfma_f32_32x32x16_bf16 v[128:143], v[156:159], v[174:177], v[128:143]
	v_cvt_pk_bf16_f32 v97, v98, v99
	v_cvt_pk_bf16_f32 v98, v100, v101
	v_cvt_pk_bf16_f32 v99, v102, v103
	s_nop 0
	v_permlane32_swap_b32_e32 v96, v98
	s_waitcnt lgkmcnt(3)
	v_mfma_f32_32x32x16_bf16 v[144:159], v[190:193], v[162:165], v[80:95]
	v_add_f32_e32 v190, v110, v111
	v_add_f32_e32 v123, v123, v190
	v_add_f32_e32 v190, v112, v113
	v_add_f32_e32 v191, v114, v115
	v_add_f32_e32 v190, v190, v191
	v_add_f32_e32 v120, v190, v120
	v_add_f32_e32 v190, v116, v117
	s_waitcnt lgkmcnt(2)
	v_mfma_f32_32x32x16_bf16 v[144:159], v[236:239], v[166:169], v[144:159]
	v_lshl_add_u32 v238, s12, 14, v221
	ds_read_b64_tr_b16 v[64:65], v238 offset:0
	ds_read_b64_tr_b16 v[66:67], v238 offset:0x800
	ds_read_b64_tr_b16 v[68:69], v238 offset:0x1000
	ds_read_b64_tr_b16 v[70:71], v238 offset:0x1800
	ds_read_b64_tr_b16 v[72:73], v238 offset:0x2000
	ds_read_b64_tr_b16 v[74:75], v238 offset:0x2800
	ds_read_b64_tr_b16 v[76:77], v238 offset:0x3000
	ds_read_b64_tr_b16 v[78:79], v238 offset:0x3800
	v_add_f32_e32 v191, v118, v119
	v_add_f32_e32 v190, v190, v191
	v_add_f32_e32 v121, v190, v121
	v_add_f32_e32 v190, v208, v209
	v_add_f32_e32 v191, v210, v211
	v_add_f32_e32 v190, v190, v191
	v_add_f32_e32 v122, v122, v190
	s_waitcnt lgkmcnt(9)
	v_mfma_f32_32x32x16_bf16 v[144:159], v[240:243], v[170:173], v[144:159]
	v_add_f32_e32 v190, v124, v125
	v_add_f32_e32 v191, v126, v127
	v_add_f32_e32 v190, v190, v191
	v_add_f32_e32 v123, v123, v190
	v_add_f32_e32 v120, v120, v121
	v_add_f32_e32 v121, v122, v123
	v_add_f32_e32 v235, v120, v121
	s_waitcnt lgkmcnt(8)
	v_mfma_f32_32x32x16_bf16 v[144:159], v[244:247], v[174:177], v[144:159]
	v_mov_b32_e32 v236, v235
	v_cvt_pk_bf16_f32 v120, v104, v105
	v_cvt_pk_bf16_f32 v121, v106, v107
	v_cvt_pk_bf16_f32 v122, v108, v109
	v_cvt_pk_bf16_f32 v123, v110, v111
	v_permlane32_swap_b32_e32 v97, v99
	v_cvt_pk_bf16_f32 v104, v112, v113
	v_cvt_pk_bf16_f32 v105, v114, v115
	v_cvt_pk_bf16_f32 v106, v116, v117
	v_cvt_pk_bf16_f32 v107, v118, v119
	s_waitcnt lgkmcnt(0)
	v_mfma_f32_32x32x16_bf16 v[0:15], v[96:99], v[64:67], v[0:15]
	v_permlane32_swap_b32_e32 v120, v122
	v_permlane32_swap_b32_e32 v121, v123
	v_cvt_pk_bf16_f32 v100, v208, v209
	v_cvt_pk_bf16_f32 v101, v210, v211
	v_cvt_pk_bf16_f32 v102, v124, v125
	v_cvt_pk_bf16_f32 v103, v126, v127
	v_mfma_f32_32x32x16_bf16 v[0:15], v[120:123], v[68:71], v[0:15]
	v_permlane32_swap_b32_e32 v104, v106
	v_permlane32_swap_b32_e32 v105, v107
	ds_read_b64_tr_b16 v[190:191], v238 offset:0x200
	ds_read_b64_tr_b16 v[192:193], v238 offset:0xa00
	ds_read_b64_tr_b16 v[240:241], v238 offset:0x1200
	ds_read_b64_tr_b16 v[242:243], v238 offset:0x1a00
	ds_read_b64_tr_b16 v[244:245], v238 offset:0x2200
	ds_read_b64_tr_b16 v[246:247], v238 offset:0x2a00
	ds_read_b64_tr_b16 v[208:209], v238 offset:0x3200
	ds_read_b64_tr_b16 v[210:211], v238 offset:0x3a00
	v_mfma_f32_32x32x16_bf16 v[0:15], v[104:107], v[72:75], v[0:15]
	v_permlane32_swap_b32_e32 v100, v102
	v_permlane32_swap_b32_e32 v101, v103
	v_permlane32_swap_b32_e32 v235, v236
	v_max_f32_e32 v108, v128, v129
	v_max3_f32 v108, v108, v144, v146
	v_max3_f32 v109, v130, v131, v145
	v_max3_f32 v108, v108, v147, v132
	v_max3_f32 v109, v109, v134, v135
	v_mfma_f32_32x32x16_bf16 v[0:15], v[100:103], v[76:79], v[0:15]
	v_max3_f32 v237, v108, v133, v148
	v_max3_f32 v239, v109, v150, v151
	ds_read_b64_tr_b16 v[124:125], v238 offset:0x400
	ds_read_b64_tr_b16 v[126:127], v238 offset:0xc00
	ds_read_b64_tr_b16 v[116:117], v238 offset:0x1400
	ds_read_b64_tr_b16 v[118:119], v238 offset:0x1c00
	ds_read_b64_tr_b16 v[112:113], v238 offset:0x2400
	ds_read_b64_tr_b16 v[114:115], v238 offset:0x2c00
	ds_read_b64_tr_b16 v[108:109], v238 offset:0x3400
	ds_read_b64_tr_b16 v[110:111], v238 offset:0x3c00
	s_waitcnt lgkmcnt(8)
	v_mfma_f32_32x32x16_bf16 v[48:63], v[96:99], v[190:193], v[48:63]
	v_max3_f32 v190, v237, v149, v136
	v_max3_f32 v191, v239, v138, v139
	v_max3_f32 v190, v190, v137, v152
	v_max3_f32 v191, v191, v154, v155
	v_max3_f32 v190, v190, v153, v140
	v_max3_f32 v191, v191, v142, v143
	v_max3_f32 v190, v190, v141, v156
	v_mfma_f32_32x32x16_bf16 v[48:63], v[120:123], v[240:243], v[48:63]
	v_max3_f32 v191, v191, v158, v159
	v_max3_f32 v190, v190, v157, v191
	v_mov_b32_e32 v191, v190
	s_nop 1
	v_permlane32_swap_b32_e32 v190, v191
	v_mfma_f32_32x32x16_bf16 v[48:63], v[104:107], v[244:247], v[48:63]
	v_max_f32_e32 v237, v190, v191
	v_mfma_f32_32x32x16_bf16 v[48:63], v[100:103], v[208:211], v[48:63]
	ds_read_b64_tr_b16 v[190:191], v238 offset:0x600
	ds_read_b64_tr_b16 v[192:193], v238 offset:0xe00
	ds_read_b64_tr_b16 v[208:209], v238 offset:0x1600
	ds_read_b64_tr_b16 v[210:211], v238 offset:0x1e00
	ds_read_b64_tr_b16 v[240:241], v238 offset:0x2600
	ds_read_b64_tr_b16 v[242:243], v238 offset:0x2e00
	ds_read_b64_tr_b16 v[244:245], v238 offset:0x3600
	ds_read_b64_tr_b16 v[246:247], v238 offset:0x3e00
	s_mov_b32 s2, 0x4138aa3b
	v_cmp_ge_f32_e32 vcc, s2, v237
	s_cmp_eq_u64 vcc, exec
	s_cbranch_scc0 .LBB0_859
	v_mov_b32_e32 v237, 1.0
